# MLA QK^T phase: tile DMA requests moved from gaps 1-3 to gaps 4-6 (first three gaps: MFMA + K reads + SALU only)
# baseline (speedup 1.0000x reference)
.LBB0_1149:
	s_setprio 1
	s_waitcnt lgkmcnt(0)
	v_mfma_f32_32x32x16_bf16 v[100:115], v[202:205], v[136:139], v[36:51]
	s_add_i32 s19, s27, -1
	s_and_b32 s18, s19, 3
	s_mul_i32 s20, s18, 0x3000
	s_and_b32 s17, s14, 0x6000
	ds_read_b128 v[202:205], v156 offset:4096
	v_mfma_f32_32x32x16_bf16 v[84:99], v[190:193], v[136:139], v[36:51]
	ds_read_b128 v[190:193], v156 offset:4608
	v_mfma_f32_32x32x16_bf16 v[100:115], v[194:197], v[132:135], v[100:115]
	ds_read_b128 v[194:197], v156 offset:6144
	v_mfma_f32_32x32x16_bf16 v[84:99], v[198:201], v[132:135], v[84:99]
	s_add_i32 s16, s27, 2
	s_min_i32 s8, s16, s2
	s_lshl_b64 s[10:11], s[8:9], 17
	v_lshl_add_u64 v[154:155], v[176:177], 0, s[10:11]
	s_and_b32 s10, s16, 3
	s_mulk_i32 s10, 0x3000
	s_add_i32 s10, s26, s10
	s_mov_b32 m0, s10
	s_nop 0
	global_load_lds_dwordx4 v[154:155], off
	ds_read_b128 v[198:201], v156 offset:6656
	v_exp_f32_e32 v60, v60
	v_exp_f32_e32 v61, v61
	v_exp_f32_e32 v62, v62
	v_exp_f32_e32 v63, v63
	s_waitcnt lgkmcnt(0)
	v_mfma_f32_32x32x16_bf16 v[100:115], v[202:205], v[128:131], v[100:115]
	s_and_b64 vcc, exec, s[38:39]
	s_cbranch_vccnz .Lmla_rope1
	s_lshl_b64 s[12:13], s[8:9], 18
	v_lshl_add_u64 v[154:155], v[180:181], 0, s[12:13]
	s_add_i32 m0, s10, 0x2000
	s_nop 0
	global_load_lds_dwordx4 v[154:155], off
.Lmla_rope1:
	ds_read_b128 v[202:205], v156 offset:8192
	v_exp_f32_e32 v64, v64
	v_exp_f32_e32 v65, v65
	v_exp_f32_e32 v66, v66
	v_exp_f32_e32 v67, v67
	v_mfma_f32_32x32x16_bf16 v[84:99], v[190:193], v[128:131], v[84:99]
	s_add_i32 s8, s27, 1
	s_min_i32 s8, s8, s2
	s_lshl_b32 s8, s8, 17
	v_lshl_add_u64 v[154:155], v[178:179], 0, s[8:9]
	s_add_i32 s8, s14, 0xffffe000
	s_and_b32 s15, s8, 0x6000
	s_add_i32 s8, s26, s15
	v_lshl_add_u64 v[154:155], v[154:155], 0, s[24:25]
	s_add_i32 m0, s8, 0xc000
	s_nop 0
	global_load_lds_dwordx4 v[154:155], off
	ds_read_b128 v[190:193], v156 offset:8704
	v_add_f32_e32 v162, v68, v69
	ds_read_b64_tr_b16 v[172:173], v157 offset:49152
	ds_read_b64_tr_b16 v[174:175], v157 offset:49664
	v_add_f32_e32 v161, v70, v162
	v_add_f32_e32 v161, v71, v161
	v_add_f32_e32 v161, v72, v161
	v_add_f32_e32 v144, v73, v161
	v_cvt_pk_bf16_f32 v140, v68, v69
	v_mfma_f32_32x32x16_bf16 v[100:115], v[194:197], v[124:127], v[100:115]
	ds_read_b128 v[194:197], v156 offset:10240
	v_cvt_pk_bf16_f32 v141, v70, v71
	ds_read_b64_tr_b16 v[68:69], v157 offset:53248
	ds_read_b64_tr_b16 v[70:71], v157 offset:53760
	v_add_f32_e32 v142, v74, v144
	v_add_f32_e32 v142, v75, v142
	v_add_f32_e32 v142, v76, v142
	v_add_f32_e32 v144, v77, v142
	v_cvt_pk_bf16_f32 v142, v72, v73
	v_mfma_f32_32x32x16_bf16 v[84:99], v[198:201], v[124:127], v[84:99]
	ds_read_b128 v[198:201], v156 offset:10752
	v_cvt_pk_bf16_f32 v143, v74, v75
	ds_read_b64_tr_b16 v[72:73], v157 offset:50176
	ds_read_b64_tr_b16 v[74:75], v157 offset:50688
	v_add_f32_e32 v144, v78, v144
	v_add_f32_e32 v144, v79, v144
	v_add_f32_e32 v144, v80, v144
	v_add_f32_e32 v148, v81, v144
	v_cvt_pk_bf16_f32 v144, v76, v77
	s_waitcnt lgkmcnt(0)
	v_mfma_f32_32x32x16_bf16 v[100:115], v[202:205], v[120:123], v[100:115]
	v_cvt_pk_bf16_f32 v145, v78, v79
	ds_read_b64_tr_b16 v[76:77], v157 offset:54272
	ds_read_b64_tr_b16 v[78:79], v157 offset:54784
	v_add_f32_e32 v146, v82, v148
	v_add_f32_e32 v146, v83, v146
	v_add_f32_e32 v146, v52, v146
	v_add_f32_e32 v148, v53, v146
	v_cvt_pk_bf16_f32 v146, v80, v81
	v_cvt_pk_bf16_f32 v147, v82, v83
	ds_read_b64_tr_b16 v[80:81], v157 offset:51200
	v_mfma_f32_32x32x16_bf16 v[84:99], v[190:193], v[120:123], v[84:99]
	ds_read_b64_tr_b16 v[82:83], v157 offset:51712
	v_add_f32_e32 v148, v54, v148
	v_add_f32_e32 v148, v55, v148
	v_add_f32_e32 v148, v56, v148
	v_add_f32_e32 v152, v57, v148
	v_cvt_pk_bf16_f32 v148, v52, v53
	v_cvt_pk_bf16_f32 v149, v54, v55
	ds_read_b64_tr_b16 v[52:53], v157 offset:55296
	ds_read_b64_tr_b16 v[54:55], v157 offset:55808
	v_add_f32_e32 v150, v58, v152
	v_mfma_f32_32x32x16_bf16 v[100:115], v[194:197], v[116:119], v[100:115]
	v_add_f32_e32 v150, v59, v150
	v_add_f32_e32 v150, v60, v150
	v_add_f32_e32 v152, v61, v150
	v_cvt_pk_bf16_f32 v150, v56, v57
	v_cvt_pk_bf16_f32 v151, v58, v59
	ds_read_b64_tr_b16 v[56:57], v157 offset:52224
	ds_read_b64_tr_b16 v[58:59], v157 offset:52736
	v_add_f32_e32 v152, v62, v152
	v_add_f32_e32 v152, v63, v152
	v_add_f32_e32 v152, v64, v152
	v_mfma_f32_32x32x16_bf16 v[84:99], v[198:201], v[116:119], v[84:99]
	v_add_f32_e32 v160, v65, v152
	v_cvt_pk_bf16_f32 v152, v60, v61
	v_cvt_pk_bf16_f32 v153, v62, v63
	ds_read_b64_tr_b16 v[60:61], v157 offset:56320
	ds_read_b64_tr_b16 v[62:63], v157 offset:56832
	v_add_f32_e32 v154, v66, v160
	v_add_f32_e32 v156, v67, v154
	v_cvt_pk_bf16_f32 v154, v64, v65
	v_cvt_pk_bf16_f32 v155, v66, v67
	s_setprio 0
	s_cmp_lt_i32 s19, s52
	s_cbranch_scc0 .LBB0_1167

.LBB0_1159:
	s_setprio 1
	s_waitcnt lgkmcnt(0)
	v_mfma_f32_32x32x16_bf16 v[68:83], v[202:205], v[136:139], v[36:51]
	ds_read_b128 v[202:205], v140 offset:4096
	v_mfma_f32_32x32x16_bf16 v[52:67], v[190:193], v[136:139], v[36:51]
	ds_read_b128 v[190:193], v140 offset:4608
	v_mfma_f32_32x32x16_bf16 v[68:83], v[194:197], v[132:135], v[68:83]
	ds_read_b128 v[194:197], v140 offset:6144
	v_mfma_f32_32x32x16_bf16 v[52:67], v[198:201], v[132:135], v[52:67]
	s_add_i32 s8, s27, 3
	s_min_i32 s8, s8, s2
	s_lshl_b64 s[10:11], s[8:9], 17
	v_lshl_add_u64 v[170:171], v[176:177], 0, s[10:11]
	s_add_i32 s10, s26, s20
	s_mov_b32 m0, s10
	s_nop 0
	global_load_lds_dwordx4 v[170:171], off
	ds_read_b128 v[198:201], v140 offset:6656
	v_exp_f32_e32 v92, v92
	v_exp_f32_e32 v93, v93
	v_exp_f32_e32 v94, v94
	v_exp_f32_e32 v95, v95
	s_waitcnt lgkmcnt(0)
	v_mfma_f32_32x32x16_bf16 v[68:83], v[202:205], v[128:131], v[68:83]
	s_and_b64 vcc, exec, s[38:39]
	s_cbranch_vccnz .Lmla_rope2
	s_lshl_b64 s[12:13], s[8:9], 18
	v_lshl_add_u64 v[170:171], v[180:181], 0, s[12:13]
	s_add_i32 m0, s10, 0x2000
	s_nop 0
	global_load_lds_dwordx4 v[170:171], off
.Lmla_rope2:
	ds_read_b128 v[202:205], v140 offset:8192
	v_exp_f32_e32 v96, v96
	v_exp_f32_e32 v97, v97
	v_exp_f32_e32 v98, v98
	v_exp_f32_e32 v99, v99
	v_mfma_f32_32x32x16_bf16 v[52:67], v[190:193], v[128:131], v[52:67]
	s_cmp_lt_u32 s19, s3
	s_cselect_b32 s8, s16, s2
	s_lshl_b64 s[10:11], s[8:9], 17
	v_lshl_add_u64 v[170:171], v[178:179], 0, s[10:11]
	s_add_i32 s8, s26, s17
	v_lshl_add_u64 v[170:171], v[170:171], 0, s[24:25]
	s_add_i32 m0, s8, 0xc000
	s_and_b32 s17, s27, 3
	global_load_lds_dwordx4 v[170:171], off
	s_mulk_i32 s17, 0x3000
	ds_read_b128 v[190:193], v140 offset:8704
	v_add_f32_e32 v147, v100, v101
	ds_read_b64_tr_b16 v[172:173], v141 offset:49152
	ds_read_b64_tr_b16 v[174:175], v141 offset:49664
	v_add_f32_e32 v146, v102, v147
	v_add_f32_e32 v146, v103, v146
	v_add_f32_e32 v146, v104, v146
	v_add_f32_e32 v144, v105, v146
	v_cvt_pk_bf16_f32 v156, v100, v101
	v_mfma_f32_32x32x16_bf16 v[68:83], v[194:197], v[124:127], v[68:83]
	ds_read_b128 v[194:197], v140 offset:10240
	v_cvt_pk_bf16_f32 v157, v102, v103
	ds_read_b64_tr_b16 v[100:101], v141 offset:53248
	ds_read_b64_tr_b16 v[102:103], v141 offset:53760
	v_add_f32_e32 v144, v106, v144
	v_add_f32_e32 v144, v107, v144
	v_add_f32_e32 v144, v108, v144
	v_add_f32_e32 v144, v109, v144
	v_cvt_pk_bf16_f32 v158, v104, v105
	v_mfma_f32_32x32x16_bf16 v[52:67], v[198:201], v[124:127], v[52:67]
	ds_read_b128 v[198:201], v140 offset:10752
	v_cvt_pk_bf16_f32 v159, v106, v107
	ds_read_b64_tr_b16 v[104:105], v141 offset:50176
	ds_read_b64_tr_b16 v[106:107], v141 offset:50688
	v_add_f32_e32 v144, v110, v144
	v_add_f32_e32 v144, v111, v144
	v_add_f32_e32 v144, v112, v144
	v_add_f32_e32 v144, v113, v144
	v_cvt_pk_bf16_f32 v160, v108, v109
	s_waitcnt lgkmcnt(0)
	v_mfma_f32_32x32x16_bf16 v[68:83], v[202:205], v[120:123], v[68:83]
	v_cvt_pk_bf16_f32 v161, v110, v111
	ds_read_b64_tr_b16 v[108:109], v141 offset:54272
	ds_read_b64_tr_b16 v[110:111], v141 offset:54784
	v_add_f32_e32 v144, v114, v144
	v_add_f32_e32 v144, v115, v144
	v_add_f32_e32 v144, v84, v144
	v_add_f32_e32 v144, v85, v144
	v_cvt_pk_bf16_f32 v162, v112, v113
	v_cvt_pk_bf16_f32 v163, v114, v115
	ds_read_b64_tr_b16 v[112:113], v141 offset:51200
	v_mfma_f32_32x32x16_bf16 v[52:67], v[190:193], v[120:123], v[52:67]
	ds_read_b64_tr_b16 v[114:115], v141 offset:51712
	v_add_f32_e32 v144, v86, v144
	v_add_f32_e32 v144, v87, v144
	v_add_f32_e32 v144, v88, v144
	v_add_f32_e32 v144, v89, v144
	v_cvt_pk_bf16_f32 v164, v84, v85
	v_cvt_pk_bf16_f32 v165, v86, v87
	ds_read_b64_tr_b16 v[84:85], v141 offset:55296
	ds_read_b64_tr_b16 v[86:87], v141 offset:55808
	v_add_f32_e32 v144, v90, v144
	v_mfma_f32_32x32x16_bf16 v[68:83], v[194:197], v[116:119], v[68:83]
	v_add_f32_e32 v144, v91, v144
	v_add_f32_e32 v144, v92, v144
	v_add_f32_e32 v144, v93, v144
	v_cvt_pk_bf16_f32 v166, v88, v89
	v_cvt_pk_bf16_f32 v167, v90, v91
	ds_read_b64_tr_b16 v[88:89], v141 offset:52224
	ds_read_b64_tr_b16 v[90:91], v141 offset:52736
	v_add_f32_e32 v144, v94, v144
	v_add_f32_e32 v144, v95, v144
	v_add_f32_e32 v144, v96, v144
	v_mfma_f32_32x32x16_bf16 v[52:67], v[198:201], v[116:119], v[52:67]
	v_add_f32_e32 v144, v97, v144
	v_cvt_pk_bf16_f32 v168, v92, v93
	v_cvt_pk_bf16_f32 v169, v94, v95
	ds_read_b64_tr_b16 v[92:93], v141 offset:56320
	ds_read_b64_tr_b16 v[94:95], v141 offset:56832
	v_add_f32_e32 v140, v98, v144
	v_add_f32_e32 v140, v99, v140
	v_cvt_pk_bf16_f32 v170, v96, v97
	v_cvt_pk_bf16_f32 v171, v98, v99
	s_setprio 0
	s_cmp_lt_i32 s27, s52
	s_cbranch_scc0 .LBB0_1171
